# input-projection tile rebalance refined: CUs 64-127 take a 7th bf16 tile from CUs 128-191, which take the spare fp8 tiles (loads 7+7 / 7+7 / 10+5 / 8+6)
# speedup vs baseline: 1.0011x; 1.0011x over previous
.LBB0_168:
	s_add_i32 s51, s51, 1
	s_mul_i32 s13, s51, s29
	s_mul_hi_u32 s15, s51, s28
	s_add_i32 s15, s15, s13
	s_mul_i32 s13, s51, s28
	s_add_u32 s16, s13, s2
	s_addc_u32 s17, s15, s3
	s_cmp_lg_u32 s28, 0x100
	s_cbranch_scc1 .Lin_rebal_skip
	s_cmp_eq_u32 s51, 7
	s_cselect_b32 s100, 128, 0
	s_cmp_lt_u32 s2, s100
	s_cselect_b32 s16, 0x800, s16
	s_sub_u32 s100, s2, 128
	s_cmp_lt_u32 s100, 64
	s_cbranch_scc0 .Lin_rebal_skip
	s_add_u32 s100, s100, 0x700
	s_cmp_eq_u32 s51, 8
	s_cselect_b32 s16, s100, s16
	s_cselect_b32 s17, 0, s17
	s_add_u32 s100, s100, 64
	s_cmp_eq_u32 s51, 9
	s_cselect_b32 s16, s100, s16
	s_cselect_b32 s17, 0, s17

.LBB0_188:
	s_add_i32 s53, s53, 1
	s_mul_i32 s11, s53, s29
	s_mul_hi_u32 s13, s53, s28
	s_add_i32 s13, s13, s11
	s_mul_i32 s11, s53, s28
	s_add_u32 s14, s11, s2
	s_addc_u32 s15, s13, s3
	s_cmp_lg_u32 s28, 0x100
	s_cbranch_scc1 .Lin16_skip
	s_sub_u32 s100, s2, 128
	s_cmp_lt_u32 s100, 64
	s_cselect_b32 s101, 5, -1
	s_cmp_eq_u32 s53, s101
	s_cselect_b32 s14, 0x640, s14
	s_cselect_b32 s15, 0, s15
	s_sub_u32 s100, s2, 64
	s_cmp_lt_u32 s100, 64
	s_cselect_b32 s101, 6, -1
	s_add_u32 s100, s2, 0x540
	s_cmp_eq_u32 s53, s101
	s_cselect_b32 s14, s100, s14
	s_cselect_b32 s15, 0, s15
.Lin16_skip:
	v_mov_b64_e32 v[4:5], 0x640
	v_cmp_lt_i64_e64 s[36:37], s[14:15], v[4:5]
	v_mov_b64_e32 v[4:5], 0x63f
	v_cmp_gt_i64_e32 vcc, s[14:15], v[4:5]
	s_cbranch_vccnz .LBB0_190
	s_ashr_i32 s10, s14, 31
	s_lshr_b32 s10, s10, 29
	s_add_i32 s10, s14, s10
	s_ashr_i32 s11, s10, 3
	s_and_b32 s10, s10, -8
	s_sub_i32 s10, s14, s10
	s_cmp_lt_i32 s10, 0
	s_movk_i32 s12, 0xc9
	s_cselect_b32 s12, s12, 0xc8
	s_mul_i32 s10, s12, s10
	s_add_i32 s10, s10, s11
	s_mul_hi_i32 s11, s10, 0x51eb851f
	s_lshr_b32 s12, s11, 31
	s_ashr_i32 s11, s11, 6
	s_add_i32 s11, s11, s12
	s_lshl_b32 s12, s11, 3
	s_sub_i32 s13, 64, s12
	s_min_i32 s13, s13, 8
	s_abs_i32 s14, s13
	v_cvt_f32_u32_e32 v4, s14
	s_sub_i32 s16, 0, s14
	s_mulk_i32 s11, 0xc8
	s_sub_i32 s11, s10, s11
	v_rcp_iflag_f32_e32 v4, v4
	s_abs_i32 s10, s11
	s_xor_b32 s15, s11, s13
	s_ashr_i32 s15, s15, 31
	v_mul_f32_e32 v4, 0x4f7ffffe, v4
	v_cvt_u32_f32_e32 v4, v4
	s_nop 0
	v_readfirstlane_b32 s17, v4
	s_mul_i32 s16, s16, s17
	s_mul_hi_u32 s16, s17, s16
	s_add_i32 s17, s17, s16
	s_mul_hi_u32 s16, s10, s17
	s_mul_i32 s17, s16, s14
	s_sub_i32 s10, s10, s17
	s_add_i32 s24, s16, 1
	s_sub_i32 s17, s10, s14
	s_cmp_ge_u32 s10, s14
	s_cselect_b32 s16, s24, s16
	s_cselect_b32 s10, s17, s10
	s_add_i32 s17, s16, 1
	s_cmp_ge_u32 s10, s14
	s_cselect_b32 s10, s17, s16
	s_xor_b32 s10, s10, s15
	s_sub_i32 s10, s10, s15
	s_mul_i32 s13, s10, s13
	s_sub_i32 s11, s11, s13
	s_add_i32 s12, s11, s12
